# v13 + hand-written out-proj EpiRes2 epilogue: residual loads all issued up front, packed f32 fma, lane-transposed coalesced stores
# speedup vs baseline: 1.0045x; 1.0014x over previous
.LBB0_1726:
	s_add_u32 s6, s46, 0x1c00000
	s_addc_u32 s7, s47, 0
	s_lshl_b32 s4, s0, 8
	s_add_i32 s0, s4, s76
	s_lshl_b32 s5, s1, 5
	s_lshl_b32 s98, s10, 8
	s_or_b32 s5, s5, s98
	s_lshl_b32 s98, s1, 2
	v_lshl_add_u32 v249, v167, 4, s98
	v_or_b32_e32 v142, s0, v146
	v_lshrrev_b32_e32 v143, 1, v248
	v_and_or_b32 v143, v143, 24, s5
	v_mov_b32_e32 v246, v142
	v_mov_b32_e32 v247, 0
	v_lshl_add_u64 v[246:247], v[246:247], 2, s[6:7]
	v_lshlrev_b32_e32 v142, 11, v142
	v_lshl_add_u32 v142, v143, 1, v142
	v_mov_b32_e32 v143, 0
	v_lshl_add_u64 v[142:143], s[60:61], 0, v[142:143]
	s_mov_b32 s98, 0x8000
	s_mov_b32 s99, 0
	s_mov_b32 s100, 0x28000
	s_mov_b32 s101, 0
	global_load_dword v214, v[246:247], off
	global_load_dword v216, v[246:247], off offset:64
	global_load_dword v218, v[246:247], off offset:128
	global_load_dword v220, v[246:247], off offset:192
	global_load_dword v222, v[246:247], off offset:512
	global_load_dword v224, v[246:247], off offset:576
	global_load_dword v226, v[246:247], off offset:640
	global_load_dword v228, v[246:247], off offset:704
	global_load_dwordx4 v[150:153], v[142:143], off
	global_load_dwordx4 v[154:157], v[142:143], off offset:256
	v_lshl_add_u64 v[142:143], v[142:143], 0, s[98:99]
	global_load_dwordx4 v[158:161], v[142:143], off
	global_load_dwordx4 v[162:165], v[142:143], off offset:256
	v_lshl_add_u64 v[142:143], v[142:143], 0, s[98:99]
	global_load_dwordx4 v[166:169], v[142:143], off
	global_load_dwordx4 v[170:173], v[142:143], off offset:256
	v_lshl_add_u64 v[142:143], v[142:143], 0, s[98:99]
	global_load_dwordx4 v[174:177], v[142:143], off
	global_load_dwordx4 v[178:181], v[142:143], off offset:256
	v_lshl_add_u64 v[142:143], v[142:143], 0, s[100:101]
	global_load_dwordx4 v[182:185], v[142:143], off
	global_load_dwordx4 v[186:189], v[142:143], off offset:256
	v_lshl_add_u64 v[142:143], v[142:143], 0, s[98:99]
	global_load_dwordx4 v[190:193], v[142:143], off
	global_load_dwordx4 v[194:197], v[142:143], off offset:256
	v_lshl_add_u64 v[142:143], v[142:143], 0, s[98:99]
	global_load_dwordx4 v[198:201], v[142:143], off
	global_load_dwordx4 v[202:205], v[142:143], off offset:256
	v_lshl_add_u64 v[142:143], v[142:143], 0, s[98:99]
	global_load_dwordx4 v[206:209], v[142:143], off
	global_load_dwordx4 v[210:213], v[142:143], off offset:256
	v_lshrrev_b32_e32 v144, 2, v248
	v_and_b32_e32 v145, 3, v248
	v_lshlrev_b32_e32 v147, 6, v145
	v_lshl_add_u32 v147, v144, 2, v147
	v_add_u32_e32 v144, s0, v144
	v_lshl_or_b32 v145, v145, 3, s5
	v_lshlrev_b32_e32 v144, 11, v144
	v_lshl_add_u32 v144, v145, 1, v144
	v_mov_b32_e32 v145, 0
	v_lshl_add_u64 v[144:145], s[60:61], 0, v[144:145]
	v_xor_b32_e32 v148, 16, v248
	v_lshlrev_b32_e32 v148, 2, v148
	v_xor_b32_e32 v149, 32, v248
	v_lshlrev_b32_e32 v149, 2, v149
	s_mov_b32 s5, 0xffff0000
	s_barrier
	s_waitcnt vmcnt(15)
	v_lshlrev_b32_e32 v134, 16, v150
	v_and_b32_e32 v135, s5, v150
	v_lshlrev_b32_e32 v136, 16, v151
	v_and_b32_e32 v137, s5, v151
	v_lshlrev_b32_e32 v138, 16, v152
	v_and_b32_e32 v139, s5, v152
	v_lshlrev_b32_e32 v140, 16, v153
	v_and_b32_e32 v141, s5, v153
	v_pk_fma_f32 v[130:131], v[214:215], v[134:135], v[130:131] op_sel_hi:[0,1,1]
	v_pk_fma_f32 v[132:133], v[214:215], v[136:137], v[132:133] op_sel_hi:[0,1,1]
	v_pk_fma_f32 v[126:127], v[214:215], v[138:139], v[126:127] op_sel_hi:[0,1,1]
	v_pk_fma_f32 v[128:129], v[214:215], v[140:141], v[128:129] op_sel_hi:[0,1,1]
	v_pk_mul_f32 v[230:231], v[130:131], v[130:131]
	v_pk_fma_f32 v[230:231], v[132:133], v[132:133], v[230:231]
	v_pk_fma_f32 v[230:231], v[126:127], v[126:127], v[230:231]
	v_pk_fma_f32 v[230:231], v[128:129], v[128:129], v[230:231]
	v_cvt_pk_bf16_f32 v130, v130, v131
	v_cvt_pk_bf16_f32 v131, v132, v133
	v_cvt_pk_bf16_f32 v132, v126, v127
	v_cvt_pk_bf16_f32 v133, v128, v129
	ds_bpermute_b32 v130, v147, v130
	ds_bpermute_b32 v131, v147, v131
	ds_bpermute_b32 v132, v147, v132
	ds_bpermute_b32 v133, v147, v133
	s_waitcnt vmcnt(14)
	v_lshlrev_b32_e32 v134, 16, v154
	v_and_b32_e32 v135, s5, v154
	v_lshlrev_b32_e32 v136, 16, v155
	v_and_b32_e32 v137, s5, v155
	v_lshlrev_b32_e32 v138, 16, v156
	v_and_b32_e32 v139, s5, v156
	v_lshlrev_b32_e32 v140, 16, v157
	v_and_b32_e32 v141, s5, v157
	v_pk_fma_f32 v[122:123], v[214:215], v[134:135], v[122:123] op_sel_hi:[0,1,1]
	v_pk_fma_f32 v[124:125], v[214:215], v[136:137], v[124:125] op_sel_hi:[0,1,1]
	v_pk_fma_f32 v[118:119], v[214:215], v[138:139], v[118:119] op_sel_hi:[0,1,1]
	v_pk_fma_f32 v[120:121], v[214:215], v[140:141], v[120:121] op_sel_hi:[0,1,1]
	v_pk_fma_f32 v[230:231], v[122:123], v[122:123], v[230:231]
	v_pk_fma_f32 v[230:231], v[124:125], v[124:125], v[230:231]
	v_pk_fma_f32 v[230:231], v[118:119], v[118:119], v[230:231]
	v_pk_fma_f32 v[230:231], v[120:121], v[120:121], v[230:231]
	v_cvt_pk_bf16_f32 v122, v122, v123
	v_cvt_pk_bf16_f32 v123, v124, v125
	v_cvt_pk_bf16_f32 v124, v118, v119
	v_cvt_pk_bf16_f32 v125, v120, v121
	ds_bpermute_b32 v122, v147, v122
	ds_bpermute_b32 v123, v147, v123
	ds_bpermute_b32 v124, v147, v124
	ds_bpermute_b32 v125, v147, v125
	s_waitcnt lgkmcnt(4)
	global_store_dwordx4 v[144:145], v[130:133], off
	s_waitcnt vmcnt(14)
	v_lshlrev_b32_e32 v134, 16, v158
	v_and_b32_e32 v135, s5, v158
	v_lshlrev_b32_e32 v136, 16, v159
	v_and_b32_e32 v137, s5, v159
	v_lshlrev_b32_e32 v138, 16, v160
	v_and_b32_e32 v139, s5, v160
	v_lshlrev_b32_e32 v140, 16, v161
	v_and_b32_e32 v141, s5, v161
	v_pk_fma_f32 v[114:115], v[216:217], v[134:135], v[114:115] op_sel_hi:[0,1,1]
	v_pk_fma_f32 v[116:117], v[216:217], v[136:137], v[116:117] op_sel_hi:[0,1,1]
	v_pk_fma_f32 v[106:107], v[216:217], v[138:139], v[106:107] op_sel_hi:[0,1,1]
	v_pk_fma_f32 v[108:109], v[216:217], v[140:141], v[108:109] op_sel_hi:[0,1,1]
	v_pk_mul_f32 v[232:233], v[114:115], v[114:115]
	v_pk_fma_f32 v[232:233], v[116:117], v[116:117], v[232:233]
	v_pk_fma_f32 v[232:233], v[106:107], v[106:107], v[232:233]
	v_pk_fma_f32 v[232:233], v[108:109], v[108:109], v[232:233]
	v_cvt_pk_bf16_f32 v114, v114, v115
	v_cvt_pk_bf16_f32 v115, v116, v117
	v_cvt_pk_bf16_f32 v116, v106, v107
	v_cvt_pk_bf16_f32 v117, v108, v109
	ds_bpermute_b32 v114, v147, v114
	ds_bpermute_b32 v115, v147, v115
	ds_bpermute_b32 v116, v147, v116
	ds_bpermute_b32 v117, v147, v117
	s_waitcnt lgkmcnt(4)
	global_store_dwordx4 v[144:145], v[122:125], off offset:256
	v_lshl_add_u64 v[144:145], v[144:145], 0, s[98:99]
	s_waitcnt vmcnt(14)
	v_lshlrev_b32_e32 v134, 16, v162
	v_and_b32_e32 v135, s5, v162
	v_lshlrev_b32_e32 v136, 16, v163
	v_and_b32_e32 v137, s5, v163
	v_lshlrev_b32_e32 v138, 16, v164
	v_and_b32_e32 v139, s5, v164
	v_lshlrev_b32_e32 v140, 16, v165
	v_and_b32_e32 v141, s5, v165
	v_pk_fma_f32 v[102:103], v[216:217], v[134:135], v[102:103] op_sel_hi:[0,1,1]
	v_pk_fma_f32 v[104:105], v[216:217], v[136:137], v[104:105] op_sel_hi:[0,1,1]
	v_pk_fma_f32 v[98:99], v[216:217], v[138:139], v[98:99] op_sel_hi:[0,1,1]
	v_pk_fma_f32 v[100:101], v[216:217], v[140:141], v[100:101] op_sel_hi:[0,1,1]
	v_pk_fma_f32 v[232:233], v[102:103], v[102:103], v[232:233]
	v_pk_fma_f32 v[232:233], v[104:105], v[104:105], v[232:233]
	v_pk_fma_f32 v[232:233], v[98:99], v[98:99], v[232:233]
	v_pk_fma_f32 v[232:233], v[100:101], v[100:101], v[232:233]
	v_cvt_pk_bf16_f32 v102, v102, v103
	v_cvt_pk_bf16_f32 v103, v104, v105
	v_cvt_pk_bf16_f32 v104, v98, v99
	v_cvt_pk_bf16_f32 v105, v100, v101
	ds_bpermute_b32 v102, v147, v102
	ds_bpermute_b32 v103, v147, v103
	ds_bpermute_b32 v104, v147, v104
	ds_bpermute_b32 v105, v147, v105
	s_waitcnt lgkmcnt(4)
	global_store_dwordx4 v[144:145], v[114:117], off
	s_waitcnt vmcnt(14)
	v_lshlrev_b32_e32 v134, 16, v166
	v_and_b32_e32 v135, s5, v166
	v_lshlrev_b32_e32 v136, 16, v167
	v_and_b32_e32 v137, s5, v167
	v_lshlrev_b32_e32 v138, 16, v168
	v_and_b32_e32 v139, s5, v168
	v_lshlrev_b32_e32 v140, 16, v169
	v_and_b32_e32 v141, s5, v169
	v_pk_fma_f32 v[94:95], v[218:219], v[134:135], v[94:95] op_sel_hi:[0,1,1]
	v_pk_fma_f32 v[96:97], v[218:219], v[136:137], v[96:97] op_sel_hi:[0,1,1]
	v_pk_fma_f32 v[90:91], v[218:219], v[138:139], v[90:91] op_sel_hi:[0,1,1]
	v_pk_fma_f32 v[92:93], v[218:219], v[140:141], v[92:93] op_sel_hi:[0,1,1]
	v_pk_mul_f32 v[234:235], v[94:95], v[94:95]
	v_pk_fma_f32 v[234:235], v[96:97], v[96:97], v[234:235]
	v_pk_fma_f32 v[234:235], v[90:91], v[90:91], v[234:235]
	v_pk_fma_f32 v[234:235], v[92:93], v[92:93], v[234:235]
	v_cvt_pk_bf16_f32 v94, v94, v95
	v_cvt_pk_bf16_f32 v95, v96, v97
	v_cvt_pk_bf16_f32 v96, v90, v91
	v_cvt_pk_bf16_f32 v97, v92, v93
	ds_bpermute_b32 v94, v147, v94
	ds_bpermute_b32 v95, v147, v95
	ds_bpermute_b32 v96, v147, v96
	ds_bpermute_b32 v97, v147, v97
	s_waitcnt lgkmcnt(4)
	global_store_dwordx4 v[144:145], v[102:105], off offset:256
	v_lshl_add_u64 v[144:145], v[144:145], 0, s[98:99]
	s_waitcnt vmcnt(14)
	v_lshlrev_b32_e32 v134, 16, v170
	v_and_b32_e32 v135, s5, v170
	v_lshlrev_b32_e32 v136, 16, v171
	v_and_b32_e32 v137, s5, v171
	v_lshlrev_b32_e32 v138, 16, v172
	v_and_b32_e32 v139, s5, v172
	v_lshlrev_b32_e32 v140, 16, v173
	v_and_b32_e32 v141, s5, v173
	v_pk_fma_f32 v[86:87], v[218:219], v[134:135], v[86:87] op_sel_hi:[0,1,1]
	v_pk_fma_f32 v[88:89], v[218:219], v[136:137], v[88:89] op_sel_hi:[0,1,1]
	v_pk_fma_f32 v[82:83], v[218:219], v[138:139], v[82:83] op_sel_hi:[0,1,1]
	v_pk_fma_f32 v[84:85], v[218:219], v[140:141], v[84:85] op_sel_hi:[0,1,1]
	v_pk_fma_f32 v[234:235], v[86:87], v[86:87], v[234:235]
	v_pk_fma_f32 v[234:235], v[88:89], v[88:89], v[234:235]
	v_pk_fma_f32 v[234:235], v[82:83], v[82:83], v[234:235]
	v_pk_fma_f32 v[234:235], v[84:85], v[84:85], v[234:235]
	v_cvt_pk_bf16_f32 v86, v86, v87
	v_cvt_pk_bf16_f32 v87, v88, v89
	v_cvt_pk_bf16_f32 v88, v82, v83
	v_cvt_pk_bf16_f32 v89, v84, v85
	ds_bpermute_b32 v86, v147, v86
	ds_bpermute_b32 v87, v147, v87
	ds_bpermute_b32 v88, v147, v88
	ds_bpermute_b32 v89, v147, v89
	s_waitcnt lgkmcnt(4)
	global_store_dwordx4 v[144:145], v[94:97], off
	s_waitcnt vmcnt(14)
	v_lshlrev_b32_e32 v134, 16, v174
	v_and_b32_e32 v135, s5, v174
	v_lshlrev_b32_e32 v136, 16, v175
	v_and_b32_e32 v137, s5, v175
	v_lshlrev_b32_e32 v138, 16, v176
	v_and_b32_e32 v139, s5, v176
	v_lshlrev_b32_e32 v140, 16, v177
	v_and_b32_e32 v141, s5, v177
	v_pk_fma_f32 v[78:79], v[220:221], v[134:135], v[78:79] op_sel_hi:[0,1,1]
	v_pk_fma_f32 v[80:81], v[220:221], v[136:137], v[80:81] op_sel_hi:[0,1,1]
	v_pk_fma_f32 v[74:75], v[220:221], v[138:139], v[74:75] op_sel_hi:[0,1,1]
	v_pk_fma_f32 v[76:77], v[220:221], v[140:141], v[76:77] op_sel_hi:[0,1,1]
	v_pk_mul_f32 v[236:237], v[78:79], v[78:79]
	v_pk_fma_f32 v[236:237], v[80:81], v[80:81], v[236:237]
	v_pk_fma_f32 v[236:237], v[74:75], v[74:75], v[236:237]
	v_pk_fma_f32 v[236:237], v[76:77], v[76:77], v[236:237]
	v_cvt_pk_bf16_f32 v78, v78, v79
	v_cvt_pk_bf16_f32 v79, v80, v81
	v_cvt_pk_bf16_f32 v80, v74, v75
	v_cvt_pk_bf16_f32 v81, v76, v77
	ds_bpermute_b32 v78, v147, v78
	ds_bpermute_b32 v79, v147, v79
	ds_bpermute_b32 v80, v147, v80
	ds_bpermute_b32 v81, v147, v81
	s_waitcnt lgkmcnt(4)
	global_store_dwordx4 v[144:145], v[86:89], off offset:256
	v_lshl_add_u64 v[144:145], v[144:145], 0, s[98:99]
	s_waitcnt vmcnt(14)
	v_lshlrev_b32_e32 v134, 16, v178
	v_and_b32_e32 v135, s5, v178
	v_lshlrev_b32_e32 v136, 16, v179
	v_and_b32_e32 v137, s5, v179
	v_lshlrev_b32_e32 v138, 16, v180
	v_and_b32_e32 v139, s5, v180
	v_lshlrev_b32_e32 v140, 16, v181
	v_and_b32_e32 v141, s5, v181
	v_pk_fma_f32 v[70:71], v[220:221], v[134:135], v[70:71] op_sel_hi:[0,1,1]
	v_pk_fma_f32 v[72:73], v[220:221], v[136:137], v[72:73] op_sel_hi:[0,1,1]
	v_pk_fma_f32 v[66:67], v[220:221], v[138:139], v[66:67] op_sel_hi:[0,1,1]
	v_pk_fma_f32 v[68:69], v[220:221], v[140:141], v[68:69] op_sel_hi:[0,1,1]
	v_pk_fma_f32 v[236:237], v[70:71], v[70:71], v[236:237]
	v_pk_fma_f32 v[236:237], v[72:73], v[72:73], v[236:237]
	v_pk_fma_f32 v[236:237], v[66:67], v[66:67], v[236:237]
	v_pk_fma_f32 v[236:237], v[68:69], v[68:69], v[236:237]
	v_cvt_pk_bf16_f32 v70, v70, v71
	v_cvt_pk_bf16_f32 v71, v72, v73
	v_cvt_pk_bf16_f32 v72, v66, v67
	v_cvt_pk_bf16_f32 v73, v68, v69
	ds_bpermute_b32 v70, v147, v70
	ds_bpermute_b32 v71, v147, v71
	ds_bpermute_b32 v72, v147, v72
	ds_bpermute_b32 v73, v147, v73
	s_waitcnt lgkmcnt(4)
	global_store_dwordx4 v[144:145], v[78:81], off
	s_waitcnt vmcnt(14)
	v_lshlrev_b32_e32 v134, 16, v182
	v_and_b32_e32 v135, s5, v182
	v_lshlrev_b32_e32 v136, 16, v183
	v_and_b32_e32 v137, s5, v183
	v_lshlrev_b32_e32 v138, 16, v184
	v_and_b32_e32 v139, s5, v184
	v_lshlrev_b32_e32 v140, 16, v185
	v_and_b32_e32 v141, s5, v185
	v_pk_fma_f32 v[62:63], v[222:223], v[134:135], v[62:63] op_sel_hi:[0,1,1]
	v_pk_fma_f32 v[64:65], v[222:223], v[136:137], v[64:65] op_sel_hi:[0,1,1]
	v_pk_fma_f32 v[58:59], v[222:223], v[138:139], v[58:59] op_sel_hi:[0,1,1]
	v_pk_fma_f32 v[60:61], v[222:223], v[140:141], v[60:61] op_sel_hi:[0,1,1]
	v_pk_mul_f32 v[238:239], v[62:63], v[62:63]
	v_pk_fma_f32 v[238:239], v[64:65], v[64:65], v[238:239]
	v_pk_fma_f32 v[238:239], v[58:59], v[58:59], v[238:239]
	v_pk_fma_f32 v[238:239], v[60:61], v[60:61], v[238:239]
	v_cvt_pk_bf16_f32 v62, v62, v63
	v_cvt_pk_bf16_f32 v63, v64, v65
	v_cvt_pk_bf16_f32 v64, v58, v59
	v_cvt_pk_bf16_f32 v65, v60, v61
	ds_bpermute_b32 v62, v147, v62
	ds_bpermute_b32 v63, v147, v63
	ds_bpermute_b32 v64, v147, v64
	ds_bpermute_b32 v65, v147, v65
	s_waitcnt lgkmcnt(4)
	global_store_dwordx4 v[144:145], v[70:73], off offset:256
	v_lshl_add_u64 v[144:145], v[144:145], 0, s[100:101]
	s_waitcnt vmcnt(14)
	v_lshlrev_b32_e32 v134, 16, v186
	v_and_b32_e32 v135, s5, v186
	v_lshlrev_b32_e32 v136, 16, v187
	v_and_b32_e32 v137, s5, v187
	v_lshlrev_b32_e32 v138, 16, v188
	v_and_b32_e32 v139, s5, v188
	v_lshlrev_b32_e32 v140, 16, v189
	v_and_b32_e32 v141, s5, v189
	v_pk_fma_f32 v[54:55], v[222:223], v[134:135], v[54:55] op_sel_hi:[0,1,1]
	v_pk_fma_f32 v[56:57], v[222:223], v[136:137], v[56:57] op_sel_hi:[0,1,1]
	v_pk_fma_f32 v[50:51], v[222:223], v[138:139], v[50:51] op_sel_hi:[0,1,1]
	v_pk_fma_f32 v[52:53], v[222:223], v[140:141], v[52:53] op_sel_hi:[0,1,1]
	v_pk_fma_f32 v[238:239], v[54:55], v[54:55], v[238:239]
	v_pk_fma_f32 v[238:239], v[56:57], v[56:57], v[238:239]
	v_pk_fma_f32 v[238:239], v[50:51], v[50:51], v[238:239]
	v_pk_fma_f32 v[238:239], v[52:53], v[52:53], v[238:239]
	v_cvt_pk_bf16_f32 v54, v54, v55
	v_cvt_pk_bf16_f32 v55, v56, v57
	v_cvt_pk_bf16_f32 v56, v50, v51
	v_cvt_pk_bf16_f32 v57, v52, v53
	ds_bpermute_b32 v54, v147, v54
	ds_bpermute_b32 v55, v147, v55
	ds_bpermute_b32 v56, v147, v56
	ds_bpermute_b32 v57, v147, v57
	s_waitcnt lgkmcnt(4)
	global_store_dwordx4 v[144:145], v[62:65], off
	s_waitcnt vmcnt(14)
	v_lshlrev_b32_e32 v134, 16, v190
	v_and_b32_e32 v135, s5, v190
	v_lshlrev_b32_e32 v136, 16, v191
	v_and_b32_e32 v137, s5, v191
	v_lshlrev_b32_e32 v138, 16, v192
	v_and_b32_e32 v139, s5, v192
	v_lshlrev_b32_e32 v140, 16, v193
	v_and_b32_e32 v141, s5, v193
	v_pk_fma_f32 v[46:47], v[224:225], v[134:135], v[46:47] op_sel_hi:[0,1,1]
	v_pk_fma_f32 v[48:49], v[224:225], v[136:137], v[48:49] op_sel_hi:[0,1,1]
	v_pk_fma_f32 v[42:43], v[224:225], v[138:139], v[42:43] op_sel_hi:[0,1,1]
	v_pk_fma_f32 v[44:45], v[224:225], v[140:141], v[44:45] op_sel_hi:[0,1,1]
	v_pk_mul_f32 v[240:241], v[46:47], v[46:47]
	v_pk_fma_f32 v[240:241], v[48:49], v[48:49], v[240:241]
	v_pk_fma_f32 v[240:241], v[42:43], v[42:43], v[240:241]
	v_pk_fma_f32 v[240:241], v[44:45], v[44:45], v[240:241]
	v_cvt_pk_bf16_f32 v46, v46, v47
	v_cvt_pk_bf16_f32 v47, v48, v49
	v_cvt_pk_bf16_f32 v48, v42, v43
	v_cvt_pk_bf16_f32 v49, v44, v45
	ds_bpermute_b32 v46, v147, v46
	ds_bpermute_b32 v47, v147, v47
	ds_bpermute_b32 v48, v147, v48
	ds_bpermute_b32 v49, v147, v49
	s_waitcnt lgkmcnt(4)
	global_store_dwordx4 v[144:145], v[54:57], off offset:256
	v_lshl_add_u64 v[144:145], v[144:145], 0, s[98:99]
	s_waitcnt vmcnt(14)
	v_lshlrev_b32_e32 v134, 16, v194
	v_and_b32_e32 v135, s5, v194
	v_lshlrev_b32_e32 v136, 16, v195
	v_and_b32_e32 v137, s5, v195
	v_lshlrev_b32_e32 v138, 16, v196
	v_and_b32_e32 v139, s5, v196
	v_lshlrev_b32_e32 v140, 16, v197
	v_and_b32_e32 v141, s5, v197
	v_pk_fma_f32 v[38:39], v[224:225], v[134:135], v[38:39] op_sel_hi:[0,1,1]
	v_pk_fma_f32 v[40:41], v[224:225], v[136:137], v[40:41] op_sel_hi:[0,1,1]
	v_pk_fma_f32 v[34:35], v[224:225], v[138:139], v[34:35] op_sel_hi:[0,1,1]
	v_pk_fma_f32 v[36:37], v[224:225], v[140:141], v[36:37] op_sel_hi:[0,1,1]
	v_pk_fma_f32 v[240:241], v[38:39], v[38:39], v[240:241]
	v_pk_fma_f32 v[240:241], v[40:41], v[40:41], v[240:241]
	v_pk_fma_f32 v[240:241], v[34:35], v[34:35], v[240:241]
	v_pk_fma_f32 v[240:241], v[36:37], v[36:37], v[240:241]
	v_cvt_pk_bf16_f32 v38, v38, v39
	v_cvt_pk_bf16_f32 v39, v40, v41
	v_cvt_pk_bf16_f32 v40, v34, v35
	v_cvt_pk_bf16_f32 v41, v36, v37
	ds_bpermute_b32 v38, v147, v38
	ds_bpermute_b32 v39, v147, v39
	ds_bpermute_b32 v40, v147, v40
	ds_bpermute_b32 v41, v147, v41
	s_waitcnt lgkmcnt(4)
	global_store_dwordx4 v[144:145], v[46:49], off
	s_waitcnt vmcnt(14)
	v_lshlrev_b32_e32 v134, 16, v198
	v_and_b32_e32 v135, s5, v198
	v_lshlrev_b32_e32 v136, 16, v199
	v_and_b32_e32 v137, s5, v199
	v_lshlrev_b32_e32 v138, 16, v200
	v_and_b32_e32 v139, s5, v200
	v_lshlrev_b32_e32 v140, 16, v201
	v_and_b32_e32 v141, s5, v201
	v_pk_fma_f32 v[30:31], v[226:227], v[134:135], v[30:31] op_sel_hi:[0,1,1]
	v_pk_fma_f32 v[32:33], v[226:227], v[136:137], v[32:33] op_sel_hi:[0,1,1]
	v_pk_fma_f32 v[26:27], v[226:227], v[138:139], v[26:27] op_sel_hi:[0,1,1]
	v_pk_fma_f32 v[28:29], v[226:227], v[140:141], v[28:29] op_sel_hi:[0,1,1]
	v_pk_mul_f32 v[242:243], v[30:31], v[30:31]
	v_pk_fma_f32 v[242:243], v[32:33], v[32:33], v[242:243]
	v_pk_fma_f32 v[242:243], v[26:27], v[26:27], v[242:243]
	v_pk_fma_f32 v[242:243], v[28:29], v[28:29], v[242:243]
	v_cvt_pk_bf16_f32 v30, v30, v31
	v_cvt_pk_bf16_f32 v31, v32, v33
	v_cvt_pk_bf16_f32 v32, v26, v27
	v_cvt_pk_bf16_f32 v33, v28, v29
	ds_bpermute_b32 v30, v147, v30
	ds_bpermute_b32 v31, v147, v31
	ds_bpermute_b32 v32, v147, v32
	ds_bpermute_b32 v33, v147, v33
	s_waitcnt lgkmcnt(4)
	global_store_dwordx4 v[144:145], v[38:41], off offset:256
	v_lshl_add_u64 v[144:145], v[144:145], 0, s[98:99]
	s_waitcnt vmcnt(14)
	v_lshlrev_b32_e32 v134, 16, v202
	v_and_b32_e32 v135, s5, v202
	v_lshlrev_b32_e32 v136, 16, v203
	v_and_b32_e32 v137, s5, v203
	v_lshlrev_b32_e32 v138, 16, v204
	v_and_b32_e32 v139, s5, v204
	v_lshlrev_b32_e32 v140, 16, v205
	v_and_b32_e32 v141, s5, v205
	v_pk_fma_f32 v[22:23], v[226:227], v[134:135], v[22:23] op_sel_hi:[0,1,1]
	v_pk_fma_f32 v[24:25], v[226:227], v[136:137], v[24:25] op_sel_hi:[0,1,1]
	v_pk_fma_f32 v[18:19], v[226:227], v[138:139], v[18:19] op_sel_hi:[0,1,1]
	v_pk_fma_f32 v[20:21], v[226:227], v[140:141], v[20:21] op_sel_hi:[0,1,1]
	v_pk_fma_f32 v[242:243], v[22:23], v[22:23], v[242:243]
	v_pk_fma_f32 v[242:243], v[24:25], v[24:25], v[242:243]
	v_pk_fma_f32 v[242:243], v[18:19], v[18:19], v[242:243]
	v_pk_fma_f32 v[242:243], v[20:21], v[20:21], v[242:243]
	v_cvt_pk_bf16_f32 v22, v22, v23
	v_cvt_pk_bf16_f32 v23, v24, v25
	v_cvt_pk_bf16_f32 v24, v18, v19
	v_cvt_pk_bf16_f32 v25, v20, v21
	ds_bpermute_b32 v22, v147, v22
	ds_bpermute_b32 v23, v147, v23
	ds_bpermute_b32 v24, v147, v24
	ds_bpermute_b32 v25, v147, v25
	s_waitcnt lgkmcnt(4)
	global_store_dwordx4 v[144:145], v[30:33], off
	s_waitcnt vmcnt(14)
	v_lshlrev_b32_e32 v134, 16, v206
	v_and_b32_e32 v135, s5, v206
	v_lshlrev_b32_e32 v136, 16, v207
	v_and_b32_e32 v137, s5, v207
	v_lshlrev_b32_e32 v138, 16, v208
	v_and_b32_e32 v139, s5, v208
	v_lshlrev_b32_e32 v140, 16, v209
	v_and_b32_e32 v141, s5, v209
	v_pk_fma_f32 v[14:15], v[228:229], v[134:135], v[14:15] op_sel_hi:[0,1,1]
	v_pk_fma_f32 v[16:17], v[228:229], v[136:137], v[16:17] op_sel_hi:[0,1,1]
	v_pk_fma_f32 v[10:11], v[228:229], v[138:139], v[10:11] op_sel_hi:[0,1,1]
	v_pk_fma_f32 v[12:13], v[228:229], v[140:141], v[12:13] op_sel_hi:[0,1,1]
	v_pk_mul_f32 v[244:245], v[14:15], v[14:15]
	v_pk_fma_f32 v[244:245], v[16:17], v[16:17], v[244:245]
	v_pk_fma_f32 v[244:245], v[10:11], v[10:11], v[244:245]
	v_pk_fma_f32 v[244:245], v[12:13], v[12:13], v[244:245]
	v_cvt_pk_bf16_f32 v14, v14, v15
	v_cvt_pk_bf16_f32 v15, v16, v17
	v_cvt_pk_bf16_f32 v16, v10, v11
	v_cvt_pk_bf16_f32 v17, v12, v13
	ds_bpermute_b32 v14, v147, v14
	ds_bpermute_b32 v15, v147, v15
	ds_bpermute_b32 v16, v147, v16
	ds_bpermute_b32 v17, v147, v17
	s_waitcnt lgkmcnt(4)
	global_store_dwordx4 v[144:145], v[22:25], off offset:256
	v_lshl_add_u64 v[144:145], v[144:145], 0, s[98:99]
	s_waitcnt vmcnt(14)
	v_lshlrev_b32_e32 v134, 16, v210
	v_and_b32_e32 v135, s5, v210
	v_lshlrev_b32_e32 v136, 16, v211
	v_and_b32_e32 v137, s5, v211
	v_lshlrev_b32_e32 v138, 16, v212
	v_and_b32_e32 v139, s5, v212
	v_lshlrev_b32_e32 v140, 16, v213
	v_and_b32_e32 v141, s5, v213
	v_pk_fma_f32 v[6:7], v[228:229], v[134:135], v[6:7] op_sel_hi:[0,1,1]
	v_pk_fma_f32 v[8:9], v[228:229], v[136:137], v[8:9] op_sel_hi:[0,1,1]
	v_pk_fma_f32 v[2:3], v[228:229], v[138:139], v[2:3] op_sel_hi:[0,1,1]
	v_pk_fma_f32 v[4:5], v[228:229], v[140:141], v[4:5] op_sel_hi:[0,1,1]
	v_pk_fma_f32 v[244:245], v[6:7], v[6:7], v[244:245]
	v_pk_fma_f32 v[244:245], v[8:9], v[8:9], v[244:245]
	v_pk_fma_f32 v[244:245], v[2:3], v[2:3], v[244:245]
	v_pk_fma_f32 v[244:245], v[4:5], v[4:5], v[244:245]
	v_cvt_pk_bf16_f32 v6, v6, v7
	v_cvt_pk_bf16_f32 v7, v8, v9
	v_cvt_pk_bf16_f32 v8, v2, v3
	v_cvt_pk_bf16_f32 v9, v4, v5
	ds_bpermute_b32 v6, v147, v6
	ds_bpermute_b32 v7, v147, v7
	ds_bpermute_b32 v8, v147, v8
	ds_bpermute_b32 v9, v147, v9
	s_waitcnt lgkmcnt(4)
	global_store_dwordx4 v[144:145], v[14:17], off
	s_waitcnt lgkmcnt(0)
	global_store_dwordx4 v[144:145], v[6:9], off offset:256
	v_add_f32_e32 v230, v230, v231
	v_add_f32_e32 v232, v232, v233
	v_add_f32_e32 v234, v234, v235
	v_add_f32_e32 v236, v236, v237
	v_add_f32_e32 v238, v238, v239
	v_add_f32_e32 v240, v240, v241
	v_add_f32_e32 v242, v242, v243
	v_add_f32_e32 v244, v244, v245
	ds_bpermute_b32 v150, v148, v230
	ds_bpermute_b32 v151, v148, v232
	ds_bpermute_b32 v152, v148, v234
	ds_bpermute_b32 v153, v148, v236
	ds_bpermute_b32 v154, v148, v238
	ds_bpermute_b32 v155, v148, v240
	ds_bpermute_b32 v156, v148, v242
	ds_bpermute_b32 v157, v148, v244
	s_waitcnt lgkmcnt(0)
	v_add_f32_e32 v230, v230, v150
	v_add_f32_e32 v232, v232, v151
	v_add_f32_e32 v234, v234, v152
	v_add_f32_e32 v236, v236, v153
	v_add_f32_e32 v238, v238, v154
	v_add_f32_e32 v240, v240, v155
	v_add_f32_e32 v242, v242, v156
	v_add_f32_e32 v244, v244, v157
	ds_bpermute_b32 v150, v149, v230
	ds_bpermute_b32 v151, v149, v232
	ds_bpermute_b32 v152, v149, v234
	ds_bpermute_b32 v153, v149, v236
	ds_bpermute_b32 v154, v149, v238
	ds_bpermute_b32 v155, v149, v240
	ds_bpermute_b32 v156, v149, v242
	ds_bpermute_b32 v157, v149, v244
	s_waitcnt lgkmcnt(0)
	v_add_f32_e32 v230, v230, v150
	v_add_f32_e32 v232, v232, v151
	v_add_f32_e32 v234, v234, v152
	v_add_f32_e32 v236, v236, v153
	v_add_f32_e32 v238, v238, v154
	v_add_f32_e32 v240, v240, v155
	v_add_f32_e32 v242, v242, v156
	v_add_f32_e32 v244, v244, v157
	v_cmp_gt_u32_e32 vcc, 16, v248
	s_and_saveexec_b64 s[0:1], vcc
	ds_write_b32 v249, v230
	ds_write_b32 v249, v232 offset:256
	ds_write_b32 v249, v234 offset:512
	ds_write_b32 v249, v236 offset:768
	ds_write_b32 v249, v238 offset:2048
	ds_write_b32 v249, v240 offset:2304
	ds_write_b32 v249, v242 offset:2560
	ds_write_b32 v249, v244 offset:2816
	s_or_b64 exec, exec, s[0:1]
	s_waitcnt lgkmcnt(0)
	s_barrier
	s_andn2_b32 s49, s49, 63
	v_or_b32_e32 v1, s49, v248
	s_movk_i32 s0, 0x100
	v_cmp_gt_i32_e32 vcc, s0, v1
	s_and_saveexec_b64 s[0:1], vcc
	s_cbranch_execz .LBB0_1744
	v_lshl_add_u32 v2, v1, 4, 0
	ds_read_b128 v[2:5], v2
	v_add_u32_e32 v6, s4, v1
	s_waitcnt lgkmcnt(1)
	v_ashrrev_i32_e32 v7, 31, v6
	s_ashr_i32 s11, s10, 31
	s_waitcnt lgkmcnt(0)
	v_mov_b32_e32 v8, v3
	v_mov_b32_e32 v9, v4
	v_mov_b32_e32 v3, v5
	v_pk_add_f32 v[2:3], v[8:9], v[2:3]
	s_nop 0
	v_add_f32_e32 v1, v2, v3
	v_lshl_add_u64 v[2:3], v[6:7], 4, s[46:47]
	v_lshl_add_u64 v[2:3], s[10:11], 2, v[2:3]
	v_add_co_u32_e32 v2, vcc, 0x1d70000, v2
	s_nop 1
	v_addc_co_u32_e32 v3, vcc, 0, v3, vcc
	global_store_dword v[2:3], v1, off
